# NA attention loop VALU diet: window mask from per-lane bit words (v_bfe_i32+v_bfi_b32), P to bf16 via v_cvt_pk_bf16_f32 (same RNE)
# baseline (speedup 1.0000x reference)
.LBB0_1292:
	s_ashr_i32 s47, s33, 4
	v_bfrev_b32_e32 v0, 0.5
	v_med3_i32 v4, s47, 4, v0
	s_lshl_b32 s1, s33, 5
	v_readfirstlane_b32 s0, v4
	s_add_i32 s48, s0, -4
	s_lshl_b32 s0, s47, 6
	s_and_b32 s46, s1, 32
	s_or_b32 s2, s0, s46
	s_bfe_u32 s9, s33, 0x30001
	s_ashr_i32 s3, s2, 31
	s_lshl_b32 s80, s9, 22
	s_lshl_b64 s[0:1], s[2:3], 11
	s_add_u32 s0, s20, s0
	s_addc_u32 s1, s21, s1
	s_lshl_b32 s34, s9, 7
	s_lshl_b32 s3, s9, 8
	s_add_u32 s0, s0, s3
	s_addc_u32 s1, s1, 0
	s_lshl_b32 s3, s9, 21
	s_add_u32 s49, s22, s80
	v_readlane_b32 s35, v255, 17
	s_addc_u32 s50, s23, 0
	s_or_b32 s9, s9, s35
	s_mul_i32 s36, s9, 0x780
	s_mov_b32 s37, s81
	s_lshl_b32 s8, s48, 1
	s_lshl_b64 s[36:37], s[36:37], 2
	s_add_u32 s35, s30, s36
	s_mov_b32 s9, s81
	s_addc_u32 s36, s31, s37
	v_lshl_add_u64 v[0:1], s[0:1], 0, v[176:177]
	v_lshlrev_b32_e32 v2, 1, v172
	v_mov_b32_e32 v3, v177
	s_lshl_b64 s[0:1], s[8:9], 12
	s_lshl_b64 s[8:9], s[8:9], 13
	v_lshl_add_u64 v[0:1], v[0:1], 0, v[2:3]
	v_or_b32_e32 v2, s46, v173
	s_add_u32 s8, s49, s8
	s_sub_i32 s98, s48, s47
	s_addk_i32 s98, 7
	s_lshl_b32 s98, s98, 9
	s_ashr_i32 s99, s98, 31
	s_add_u32 s98, s35, s98
	s_addc_u32 s99, s36, s99
	global_load_dwordx4 v[232:235], v198, s[98:99]
	global_load_dwordx4 v[236:239], v198, s[98:99] offset:1024
	global_load_dwordx4 v[240:243], v198, s[98:99] offset:2048
	global_load_dwordx4 v[244:247], v198, s[98:99] offset:3072
	global_load_dwordx4 v[108:111], v[0:1], off
	global_load_dwordx4 v[104:107], v[0:1], off offset:32
	global_load_dwordx4 v[100:103], v[0:1], off offset:64
	global_load_dwordx4 v[96:99], v[0:1], off offset:96
	global_load_dwordx4 v[92:95], v[0:1], off offset:128
	global_load_dwordx4 v[88:91], v[0:1], off offset:160
	global_load_dwordx4 v[84:87], v[0:1], off offset:192
	global_load_dwordx4 v[80:83], v[0:1], off offset:224
	v_min_u32_e32 v0, 56, v2
	s_addc_u32 s9, s50, s9
	v_mov_b32_e32 v199, v177
	v_sub_u32_e32 v3, 8, v0
	v_lshl_add_u64 v[0:1], s[8:9], 0, v[198:199]
	v_add_co_u32_e32 v0, vcc, s90, v0
	global_load_dwordx4 v[64:67], v198, s[8:9]
	global_load_dwordx4 v[168:171], v198, s[8:9] offset:1024
	global_load_dwordx4 v[164:167], v198, s[8:9] offset:2048
	global_load_dwordx4 v[160:163], v198, s[8:9] offset:3072
	v_addc_co_u32_e32 v1, vcc, 0, v1, vcc
	global_load_dwordx4 v[156:159], v[0:1], off
	global_load_dwordx4 v[152:155], v[0:1], off offset:1024
	global_load_dwordx4 v[148:151], v[0:1], off offset:2048
	global_load_dwordx4 v[144:147], v[0:1], off offset:3072
	v_cmp_lt_u32_e32 vcc, 7, v2
	v_mov_b32_e32 v1, v177
	v_mov_b32_e32 v207, 0
	v_cndmask_b32_e32 v0, 0, v3, vcc
	v_add_u32_e32 v201, v0, v172
	v_lshlrev_b32_e32 v0, 14, v4
	v_add_u32_e32 v0, 0xffff0000, v0
	v_lshl_add_u64 v[0:1], s[80:81], 0, v[0:1]
	s_mov_b32 s46, 0
	s_sub_i32 s37, s48, s47
	v_sub_u32_e32 v199, v208, v2
	v_lshl_add_u64 v[204:205], v[174:175], 0, v[0:1]
	v_mov_b32_e32 v206, 0xff61b1e6
	s_mov_b64 s[8:9], 0
	s_mov_b32 s47, 0
	v_mov_b32_e32 v0, 0
	v_mov_b32_e32 v1, v207
	v_mov_b32_e32 v2, v207
	v_mov_b32_e32 v3, v207
	v_mov_b32_e32 v4, v207
	v_mov_b32_e32 v5, v207
	v_mov_b32_e32 v6, v207
	v_mov_b32_e32 v7, v207
	s_waitcnt vmcnt(16)
	v_mov_b32_e32 v8, v207
	v_mov_b32_e32 v9, v207
	v_mov_b32_e32 v10, v207
	v_mov_b32_e32 v11, v207
	v_mov_b32_e32 v12, v207
	v_mov_b32_e32 v13, v207
	v_mov_b32_e32 v14, v207
	v_mov_b32_e32 v15, v207
	v_mov_b32_e32 v16, 0
	v_mov_b32_e32 v17, v207
	v_mov_b32_e32 v18, v207
	v_mov_b32_e32 v19, v207
	v_mov_b32_e32 v20, v207
	v_mov_b32_e32 v21, v207
	v_mov_b32_e32 v22, v207
	v_mov_b32_e32 v23, v207
	v_mov_b32_e32 v24, v207
	v_mov_b32_e32 v25, v207
	v_mov_b32_e32 v26, v207
	v_mov_b32_e32 v27, v207
	v_mov_b32_e32 v28, v207
	v_mov_b32_e32 v29, v207
	v_mov_b32_e32 v30, v207
	v_mov_b32_e32 v31, v207
	v_mov_b32_e32 v32, 0
	v_mov_b32_e32 v33, v207
	v_mov_b32_e32 v34, v207
	v_mov_b32_e32 v35, v207
	v_mov_b32_e32 v36, v207
	v_mov_b32_e32 v37, v207
	v_mov_b32_e32 v38, v207
	v_mov_b32_e32 v39, v207
	v_mov_b32_e32 v40, v207
	v_mov_b32_e32 v41, v207
	v_mov_b32_e32 v42, v207
	v_mov_b32_e32 v43, v207
	v_mov_b32_e32 v44, v207
	v_mov_b32_e32 v45, v207
	v_mov_b32_e32 v46, v207
	v_mov_b32_e32 v47, v207
	v_mov_b32_e32 v48, 0
	v_mov_b32_e32 v49, v207
	v_mov_b32_e32 v50, v207
	v_mov_b32_e32 v51, v207
	v_mov_b32_e32 v52, v207
	v_mov_b32_e32 v53, v207
	v_mov_b32_e32 v54, v207
	v_mov_b32_e32 v55, v207
	v_mov_b32_e32 v56, v207
	v_mov_b32_e32 v57, v207
	v_mov_b32_e32 v58, v207
	v_mov_b32_e32 v59, v207
	v_mov_b32_e32 v60, v207
	v_mov_b32_e32 v61, v207
	v_mov_b32_e32 v62, v207
	v_mov_b32_e32 v63, v207
	s_and_b32 s99, s33, 7
	s_lshl_b32 s99, s99, 12
	v_add_u32_e32 v249, s99, v198
	ds_write_b128 v249, v[232:235]
	ds_write_b128 v249, v[236:239] offset:1024
	ds_write_b128 v249, v[240:243] offset:2048
	ds_write_b128 v249, v[244:247] offset:3072
	s_lshr_b32 s98, s47, 1
	s_lshl_b32 s98, s98, 9
	s_add_i32 s98, s98, s99
	s_and_b32 s50, s46, 32
	v_add_lshl_u32 v248, s50, v199, 2
	v_add_u32_e32 v249, s98, v248
	ds_read2_b32 v[232:233], v249 offset1:1
	ds_read2_b32 v[234:235], v249 offset0:2 offset1:3
	ds_read2_b32 v[236:237], v249 offset0:4 offset1:5
	ds_read2_b32 v[238:239], v249 offset0:6 offset1:7
	ds_read2_b32 v[240:241], v249 offset0:16 offset1:17
	ds_read2_b32 v[242:243], v249 offset0:18 offset1:19
	ds_read2_b32 v[244:245], v249 offset0:20 offset1:21
	ds_read2_b32 v[246:247], v249 offset0:22 offset1:23
	s_waitcnt lgkmcnt(0)
	v_mov_b32_e32 v187, 0
	v_mov_b32_e32 v188, 0
	v_add_u32_e32 v189, 0, v201
	v_lshrrev_b32_e32 v189, 4, v189
	v_min_u32_e32 v189, 1, v189
	v_xor_b32_e32 v189, 1, v189
	v_lshl_or_b32 v187, v189, 0, v187
	v_add_u32_e32 v189, 1, v201
	v_lshrrev_b32_e32 v189, 4, v189
	v_min_u32_e32 v189, 1, v189
	v_xor_b32_e32 v189, 1, v189
	v_lshl_or_b32 v187, v189, 1, v187
	v_add_u32_e32 v189, 2, v201
	v_lshrrev_b32_e32 v189, 4, v189
	v_min_u32_e32 v189, 1, v189
	v_xor_b32_e32 v189, 1, v189
	v_lshl_or_b32 v187, v189, 2, v187
	v_add_u32_e32 v189, 3, v201
	v_lshrrev_b32_e32 v189, 4, v189
	v_min_u32_e32 v189, 1, v189
	v_xor_b32_e32 v189, 1, v189
	v_lshl_or_b32 v187, v189, 3, v187
	v_add_u32_e32 v189, 4, v201
	v_lshrrev_b32_e32 v189, 4, v189
	v_min_u32_e32 v189, 1, v189
	v_xor_b32_e32 v189, 1, v189
	v_lshl_or_b32 v187, v189, 4, v187
	v_add_u32_e32 v189, 5, v201
	v_lshrrev_b32_e32 v189, 4, v189
	v_min_u32_e32 v189, 1, v189
	v_xor_b32_e32 v189, 1, v189
	v_lshl_or_b32 v187, v189, 5, v187
	v_add_u32_e32 v189, 6, v201
	v_lshrrev_b32_e32 v189, 4, v189
	v_min_u32_e32 v189, 1, v189
	v_xor_b32_e32 v189, 1, v189
	v_lshl_or_b32 v187, v189, 6, v187
	v_add_u32_e32 v189, 7, v201
	v_lshrrev_b32_e32 v189, 4, v189
	v_min_u32_e32 v189, 1, v189
	v_xor_b32_e32 v189, 1, v189
	v_lshl_or_b32 v187, v189, 7, v187
	v_add_u32_e32 v189, 16, v201
	v_lshrrev_b32_e32 v189, 4, v189
	v_min_u32_e32 v189, 1, v189
	v_xor_b32_e32 v189, 1, v189
	v_lshl_or_b32 v187, v189, 8, v187
	v_add_u32_e32 v189, 17, v201
	v_lshrrev_b32_e32 v189, 4, v189
	v_min_u32_e32 v189, 1, v189
	v_xor_b32_e32 v189, 1, v189
	v_lshl_or_b32 v187, v189, 9, v187
	v_add_u32_e32 v189, 18, v201
	v_lshrrev_b32_e32 v189, 4, v189
	v_min_u32_e32 v189, 1, v189
	v_xor_b32_e32 v189, 1, v189
	v_lshl_or_b32 v187, v189, 10, v187
	v_add_u32_e32 v189, 19, v201
	v_lshrrev_b32_e32 v189, 4, v189
	v_min_u32_e32 v189, 1, v189
	v_xor_b32_e32 v189, 1, v189
	v_lshl_or_b32 v187, v189, 11, v187
	v_add_u32_e32 v189, 20, v201
	v_lshrrev_b32_e32 v189, 4, v189
	v_min_u32_e32 v189, 1, v189
	v_xor_b32_e32 v189, 1, v189
	v_lshl_or_b32 v187, v189, 12, v187
	v_add_u32_e32 v189, 21, v201
	v_lshrrev_b32_e32 v189, 4, v189
	v_min_u32_e32 v189, 1, v189
	v_xor_b32_e32 v189, 1, v189
	v_lshl_or_b32 v187, v189, 13, v187
	v_add_u32_e32 v189, 22, v201
	v_lshrrev_b32_e32 v189, 4, v189
	v_min_u32_e32 v189, 1, v189
	v_xor_b32_e32 v189, 1, v189
	v_lshl_or_b32 v187, v189, 14, v187
	v_add_u32_e32 v189, 23, v201
	v_lshrrev_b32_e32 v189, 4, v189
	v_min_u32_e32 v189, 1, v189
	v_xor_b32_e32 v189, 1, v189
	v_lshl_or_b32 v187, v189, 15, v187
	v_add_u32_e32 v189, 32, v201
	v_lshrrev_b32_e32 v189, 4, v189
	v_min_u32_e32 v189, 1, v189
	v_xor_b32_e32 v189, 1, v189
	v_lshl_or_b32 v188, v189, 0, v188
	v_add_u32_e32 v189, 33, v201
	v_lshrrev_b32_e32 v189, 4, v189
	v_min_u32_e32 v189, 1, v189
	v_xor_b32_e32 v189, 1, v189
	v_lshl_or_b32 v188, v189, 1, v188
	v_add_u32_e32 v189, 34, v201
	v_lshrrev_b32_e32 v189, 4, v189
	v_min_u32_e32 v189, 1, v189
	v_xor_b32_e32 v189, 1, v189
	v_lshl_or_b32 v188, v189, 2, v188
	v_add_u32_e32 v189, 35, v201
	v_lshrrev_b32_e32 v189, 4, v189
	v_min_u32_e32 v189, 1, v189
	v_xor_b32_e32 v189, 1, v189
	v_lshl_or_b32 v188, v189, 3, v188
	v_add_u32_e32 v189, 36, v201
	v_lshrrev_b32_e32 v189, 4, v189
	v_min_u32_e32 v189, 1, v189
	v_xor_b32_e32 v189, 1, v189
	v_lshl_or_b32 v188, v189, 4, v188
	v_add_u32_e32 v189, 37, v201
	v_lshrrev_b32_e32 v189, 4, v189
	v_min_u32_e32 v189, 1, v189
	v_xor_b32_e32 v189, 1, v189
	v_lshl_or_b32 v188, v189, 5, v188
	v_add_u32_e32 v189, 38, v201
	v_lshrrev_b32_e32 v189, 4, v189
	v_min_u32_e32 v189, 1, v189
	v_xor_b32_e32 v189, 1, v189
	v_lshl_or_b32 v188, v189, 6, v188
	v_add_u32_e32 v189, 39, v201
	v_lshrrev_b32_e32 v189, 4, v189
	v_min_u32_e32 v189, 1, v189
	v_xor_b32_e32 v189, 1, v189
	v_lshl_or_b32 v188, v189, 7, v188
	v_add_u32_e32 v189, 48, v201
	v_lshrrev_b32_e32 v189, 4, v189
	v_min_u32_e32 v189, 1, v189
	v_xor_b32_e32 v189, 1, v189
	v_lshl_or_b32 v188, v189, 8, v188
	v_add_u32_e32 v189, 49, v201
	v_lshrrev_b32_e32 v189, 4, v189
	v_min_u32_e32 v189, 1, v189
	v_xor_b32_e32 v189, 1, v189
	v_lshl_or_b32 v188, v189, 9, v188
	v_add_u32_e32 v189, 50, v201
	v_lshrrev_b32_e32 v189, 4, v189
	v_min_u32_e32 v189, 1, v189
	v_xor_b32_e32 v189, 1, v189
	v_lshl_or_b32 v188, v189, 10, v188
	v_add_u32_e32 v189, 51, v201
	v_lshrrev_b32_e32 v189, 4, v189
	v_min_u32_e32 v189, 1, v189
	v_xor_b32_e32 v189, 1, v189
	v_lshl_or_b32 v188, v189, 11, v188
	v_add_u32_e32 v189, 52, v201
	v_lshrrev_b32_e32 v189, 4, v189
	v_min_u32_e32 v189, 1, v189
	v_xor_b32_e32 v189, 1, v189
	v_lshl_or_b32 v188, v189, 12, v188
	v_add_u32_e32 v189, 53, v201
	v_lshrrev_b32_e32 v189, 4, v189
	v_min_u32_e32 v189, 1, v189
	v_xor_b32_e32 v189, 1, v189
	v_lshl_or_b32 v188, v189, 13, v188
	v_add_u32_e32 v189, 54, v201
	v_lshrrev_b32_e32 v189, 4, v189
	v_min_u32_e32 v189, 1, v189
	v_xor_b32_e32 v189, 1, v189
	v_lshl_or_b32 v188, v189, 14, v188
	v_add_u32_e32 v189, 55, v201
	v_lshrrev_b32_e32 v189, 4, v189
	v_min_u32_e32 v189, 1, v189
	v_xor_b32_e32 v189, 1, v189
	v_lshl_or_b32 v188, v189, 15, v188
.LBB0_1293:
	v_mov_b32_e32 v203, v207
	v_mov_b32_e32 v209, v206
	v_lshl_add_u64 v[206:207], v[204:205], 0, s[8:9]
	s_mov_b32 s48, 0x35000000
	v_add_co_u32_e32 v68, vcc, s48, v206
	s_mov_b32 s48, 0x35001000
	s_nop 0
	v_addc_co_u32_e32 v69, vcc, 0, v207, vcc
	v_add_co_u32_e32 v70, vcc, s48, v206
	s_lshr_b32 s48, s47, 1
	s_add_i32 s48, s48, s37
	s_lshl_b32 s48, s48, 7
	s_ashr_i32 s49, s48, 31
	s_lshl_b64 s[48:49], s[48:49], 2
	s_add_u32 s48, s35, s48
	v_addc_co_u32_e32 v71, vcc, 0, v207, vcc
	s_addc_u32 s49, s36, s49
	s_and_b32 s50, s46, 32
	global_load_dwordx4 v[136:139], v[70:71], off offset:-4096
	global_load_dwordx4 v[140:143], v[68:69], off offset:1024
	global_load_dwordx4 v[128:131], v[68:69], off offset:2048
	global_load_dwordx4 v[132:135], v[68:69], off offset:3072
	global_load_dwordx4 v[120:123], v[70:71], off
	global_load_dwordx4 v[124:127], v[70:71], off offset:1024
	global_load_dwordx4 v[112:115], v[70:71], off offset:2048
	global_load_dwordx4 v[116:119], v[70:71], off offset:3072
	s_waitcnt vmcnt(15)
	v_mfma_f32_32x32x16_bf16 v[64:79], v[64:67], v[108:111], 0
	s_movk_i32 s48, 0xffef
	s_add_i32 s47, s47, 1
	s_add_u32 s8, s8, 0x2000
	s_addc_u32 s9, s9, 0
	s_add_i32 s46, s46, 32
	s_waitcnt vmcnt(14)
	v_mfma_f32_32x32x16_bf16 v[64:79], v[168:171], v[104:107], v[64:79]
	s_waitcnt vmcnt(13)
	v_mfma_f32_32x32x16_bf16 v[64:79], v[164:167], v[100:103], v[64:79]
	s_waitcnt vmcnt(12)
	v_mfma_f32_32x32x16_bf16 v[64:79], v[160:163], v[96:99], v[64:79]
	s_waitcnt vmcnt(11)
	v_mfma_f32_32x32x16_bf16 v[64:79], v[156:159], v[92:95], v[64:79]
	v_add_u32_e32 v156, s50, v201
	v_cmp_gt_u32_e32 vcc, 16, v156
	s_waitcnt vmcnt(10)
	v_mfma_f32_32x32x16_bf16 v[64:79], v[152:155], v[88:91], v[64:79]
	s_waitcnt vmcnt(9)
	v_mfma_f32_32x32x16_bf16 v[64:79], v[148:151], v[84:87], v[64:79]
	s_waitcnt vmcnt(8)
	v_mfma_f32_32x32x16_bf16 v[64:79], v[144:147], v[80:83], v[64:79]
	s_nop 3
	s_nop 7
	v_bfe_i32 v178, v187, 0, 1
	v_add_f32_e32 v179, v64, v232
	v_bfi_b32 v217, v178, v179, v222
	v_bfe_i32 v180, v187, 1, 1
	v_add_f32_e32 v181, v65, v233
	v_bfi_b32 v216, v180, v181, v222
	v_bfe_i32 v178, v187, 2, 1
	v_add_f32_e32 v179, v66, v234
	v_bfi_b32 v215, v178, v179, v222
	v_bfe_i32 v180, v187, 3, 1
	v_add_f32_e32 v181, v67, v235
	v_bfi_b32 v214, v180, v181, v222
	v_bfe_i32 v178, v187, 4, 1
	v_add_f32_e32 v179, v68, v236
	v_bfi_b32 v213, v178, v179, v222
	v_bfe_i32 v180, v187, 5, 1
	v_add_f32_e32 v181, v69, v237
	v_bfi_b32 v212, v180, v181, v222
	v_bfe_i32 v178, v187, 6, 1
	v_add_f32_e32 v179, v70, v238
	v_bfi_b32 v211, v178, v179, v222
	v_bfe_i32 v180, v187, 7, 1
	v_add_f32_e32 v181, v71, v239
	v_bfi_b32 v210, v180, v181, v222
	v_bfe_i32 v178, v187, 8, 1
	v_add_f32_e32 v179, v72, v240
	v_bfi_b32 v221, v178, v179, v222
	v_bfe_i32 v180, v187, 9, 1
	v_add_f32_e32 v181, v73, v241
	v_bfi_b32 v220, v180, v181, v222
	v_bfe_i32 v178, v187, 10, 1
	v_add_f32_e32 v179, v74, v242
	v_bfi_b32 v219, v178, v179, v222
	v_bfe_i32 v180, v187, 11, 1
	v_add_f32_e32 v181, v75, v243
	v_bfi_b32 v218, v180, v181, v222
	v_bfe_i32 v178, v187, 12, 1
	v_add_f32_e32 v179, v76, v244
	v_bfi_b32 v75, v178, v179, v222
	v_bfe_i32 v180, v187, 13, 1
	v_add_f32_e32 v181, v77, v245
	v_bfi_b32 v74, v180, v181, v222
	v_bfe_i32 v178, v187, 14, 1
	v_add_f32_e32 v179, v78, v246
	v_bfi_b32 v73, v178, v179, v222
	v_bfe_i32 v180, v187, 15, 1
	v_add_f32_e32 v181, v79, v247
	v_bfi_b32 v72, v180, v181, v222
	s_mov_b32 s48, 0x33002000
	v_swap_b32 v187, v188
	s_lshr_b32 s98, s47, 1
	s_lshl_b32 s98, s98, 9
	s_add_i32 s98, s98, s99
	s_and_b32 s50, s46, 32
	v_add_lshl_u32 v248, s50, v199, 2
	v_add_u32_e32 v249, s98, v248
	ds_read2_b32 v[232:233], v249 offset1:1
	ds_read2_b32 v[234:235], v249 offset0:2 offset1:3
	ds_read2_b32 v[236:237], v249 offset0:4 offset1:5
	ds_read2_b32 v[238:239], v249 offset0:6 offset1:7
	ds_read2_b32 v[240:241], v249 offset0:16 offset1:17
	ds_read2_b32 v[242:243], v249 offset0:18 offset1:19
	ds_read2_b32 v[244:245], v249 offset0:20 offset1:21
	ds_read2_b32 v[246:247], v249 offset0:22 offset1:23
	s_cmp_lg_u32 s8, 0x1e000
	v_add_co_u32_e32 v68, vcc, s48, v206
	s_mov_b32 s48, 0x33003000
	s_nop 0
	v_addc_co_u32_e32 v69, vcc, 0, v207, vcc
	v_add_co_u32_e32 v70, vcc, s48, v206
	s_nop 1
	v_addc_co_u32_e32 v71, vcc, 0, v207, vcc
	global_load_dwordx4 v[64:67], v[70:71], off offset:-4096
	global_load_dwordx4 v[168:171], v[68:69], off offset:1024
	global_load_dwordx4 v[164:167], v[68:69], off offset:2048
	global_load_dwordx4 v[160:163], v[68:69], off offset:3072
	global_load_dwordx4 v[156:159], v[70:71], off
	global_load_dwordx4 v[152:155], v[70:71], off offset:1024
	global_load_dwordx4 v[148:151], v[70:71], off offset:2048
	global_load_dwordx4 v[144:147], v[70:71], off offset:3072
	v_max3_f32 v68, v217, s11, v216
	v_max3_f32 v68, v68, v215, v214
	v_max3_f32 v68, v68, v213, v212
	v_max3_f32 v68, v68, v211, v210
	v_max3_f32 v68, v68, v221, v220
	v_max3_f32 v68, v68, v219, v218
	v_mbcnt_lo_u32_b32 v69, -1, 0
	v_mbcnt_hi_u32_b32 v69, -1, v69
	v_max3_f32 v68, v68, v75, v74
	v_lshlrev_b32_e32 v69, 2, v69
	v_max3_f32 v68, v68, v73, v72
	v_xor_b32_e32 v69, 0x80, v69
	ds_bpermute_b32 v69, v69, v68
	s_waitcnt lgkmcnt(0)
	v_max3_f32 v206, v209, v68, v69
	v_sub_f32_e32 v69, v217, v206
	v_exp_f32_e32 v69, v69
	v_sub_f32_e32 v70, v216, v206
	v_exp_f32_e32 v70, v70
	v_sub_f32_e32 v71, v215, v206
	v_exp_f32_e32 v71, v71
	v_sub_f32_e32 v76, v214, v206
	v_exp_f32_e32 v76, v76
	v_sub_f32_e32 v77, v213, v206
	v_sub_f32_e32 v72, v72, v206
	v_exp_f32_e32 v77, v77
	v_sub_f32_e32 v78, v212, v206
	v_exp_f32_e32 v184, v72
	v_add_f32_e32 v72, 0, v69
	v_exp_f32_e32 v78, v78
	v_sub_f32_e32 v79, v211, v206
	v_add_f32_e32 v72, v70, v72
	v_exp_f32_e32 v79, v79
	v_sub_f32_e32 v178, v210, v206
	v_add_f32_e32 v72, v71, v72
	v_exp_f32_e32 v178, v178
	v_sub_f32_e32 v179, v221, v206
	v_add_f32_e32 v72, v76, v72
	v_exp_f32_e32 v179, v179
	v_sub_f32_e32 v180, v220, v206
	v_add_f32_e32 v72, v77, v72
	v_exp_f32_e32 v180, v180
	v_sub_f32_e32 v181, v219, v206
	v_add_f32_e32 v72, v78, v72
	v_exp_f32_e32 v181, v181
	v_sub_f32_e32 v182, v218, v206
	v_add_f32_e32 v72, v79, v72
	v_exp_f32_e32 v182, v182
	v_sub_f32_e32 v75, v75, v206
	v_add_f32_e32 v72, v178, v72
	v_exp_f32_e32 v75, v75
	v_sub_f32_e32 v74, v74, v206
	v_add_f32_e32 v72, v179, v72
	v_exp_f32_e32 v74, v74
	v_sub_f32_e32 v73, v73, v206
	v_add_f32_e32 v72, v180, v72
	v_exp_f32_e32 v183, v73
	v_add_f32_e32 v72, v181, v72
	v_add_f32_e32 v72, v182, v72
	v_sub_f32_e32 v68, v209, v206
	v_add_f32_e32 v72, v75, v72
	v_exp_f32_e32 v68, v68
	v_add_f32_e32 v72, v74, v72
	v_add_f32_e32 v72, v183, v72
	v_add_f32_e32 v207, v184, v72
	v_cvt_pk_bf16_f32 v70, v69, v70
	v_cvt_pk_bf16_f32 v71, v71, v76
	v_cvt_pk_bf16_f32 v72, v77, v78
	v_cvt_pk_bf16_f32 v73, v79, v178
	v_pk_mul_f32 v[62:63], v[62:63], v[68:69] op_sel_hi:[1,0]
	v_pk_mul_f32 v[60:61], v[60:61], v[68:69] op_sel_hi:[1,0]
	v_pk_mul_f32 v[58:59], v[58:59], v[68:69] op_sel_hi:[1,0]
	v_pk_mul_f32 v[56:57], v[56:57], v[68:69] op_sel_hi:[1,0]
	v_pk_mul_f32 v[54:55], v[54:55], v[68:69] op_sel_hi:[1,0]
	v_pk_mul_f32 v[52:53], v[52:53], v[68:69] op_sel_hi:[1,0]
	v_pk_mul_f32 v[50:51], v[50:51], v[68:69] op_sel_hi:[1,0]
	v_pk_mul_f32 v[48:49], v[48:49], v[68:69] op_sel_hi:[1,0]
	v_pk_mul_f32 v[46:47], v[46:47], v[68:69] op_sel_hi:[1,0]
	v_pk_mul_f32 v[44:45], v[44:45], v[68:69] op_sel_hi:[1,0]
	v_pk_mul_f32 v[42:43], v[42:43], v[68:69] op_sel_hi:[1,0]
	v_pk_mul_f32 v[40:41], v[40:41], v[68:69] op_sel_hi:[1,0]
	v_pk_mul_f32 v[38:39], v[38:39], v[68:69] op_sel_hi:[1,0]
	v_pk_mul_f32 v[36:37], v[36:37], v[68:69] op_sel_hi:[1,0]
	v_pk_mul_f32 v[34:35], v[34:35], v[68:69] op_sel_hi:[1,0]
	v_pk_mul_f32 v[32:33], v[32:33], v[68:69] op_sel_hi:[1,0]
	v_pk_mul_f32 v[30:31], v[30:31], v[68:69] op_sel_hi:[1,0]
	v_pk_mul_f32 v[28:29], v[28:29], v[68:69] op_sel_hi:[1,0]
	v_pk_mul_f32 v[26:27], v[26:27], v[68:69] op_sel_hi:[1,0]
	v_pk_mul_f32 v[24:25], v[24:25], v[68:69] op_sel_hi:[1,0]
	v_pk_mul_f32 v[22:23], v[22:23], v[68:69] op_sel_hi:[1,0]
	v_pk_mul_f32 v[20:21], v[20:21], v[68:69] op_sel_hi:[1,0]
	v_pk_mul_f32 v[18:19], v[18:19], v[68:69] op_sel_hi:[1,0]
	v_pk_mul_f32 v[16:17], v[16:17], v[68:69] op_sel_hi:[1,0]
	v_pk_mul_f32 v[14:15], v[14:15], v[68:69] op_sel_hi:[1,0]
	v_pk_mul_f32 v[12:13], v[12:13], v[68:69] op_sel_hi:[1,0]
	v_pk_mul_f32 v[10:11], v[10:11], v[68:69] op_sel_hi:[1,0]
	v_pk_mul_f32 v[8:9], v[8:9], v[68:69] op_sel_hi:[1,0]
	v_pk_mul_f32 v[6:7], v[6:7], v[68:69] op_sel_hi:[1,0]
	v_pk_mul_f32 v[4:5], v[4:5], v[68:69] op_sel_hi:[1,0]
	v_pk_mul_f32 v[2:3], v[2:3], v[68:69] op_sel_hi:[1,0]
	v_pk_mul_f32 v[0:1], v[0:1], v[68:69] op_sel_hi:[1,0]
	s_waitcnt vmcnt(8)
	v_mfma_f32_32x32x16_bf16 v[48:63], v[136:139], v[70:73], v[48:63]
	v_cvt_pk_bf16_f32 v76, v75, v74
	v_cvt_pk_bf16_f32 v74, v179, v180
	v_cvt_pk_bf16_f32 v75, v181, v182
	v_cvt_pk_bf16_f32 v77, v183, v184
	v_mfma_f32_32x32x16_bf16 v[32:47], v[128:131], v[70:73], v[32:47]
	v_mfma_f32_32x32x16_bf16 v[16:31], v[120:123], v[70:73], v[16:31]
	v_mfma_f32_32x32x16_bf16 v[0:15], v[112:115], v[70:73], v[0:15]
	v_fmac_f32_e32 v207, v203, v68
	s_nop 0
	v_mfma_f32_32x32x16_bf16 v[48:63], v[140:143], v[74:77], v[48:63]
	v_mfma_f32_32x32x16_bf16 v[32:47], v[132:135], v[74:77], v[32:47]
	v_mfma_f32_32x32x16_bf16 v[16:31], v[124:127], v[74:77], v[16:31]
	v_mfma_f32_32x32x16_bf16 v[0:15], v[116:119], v[74:77], v[0:15]
	s_cbranch_scc1 .LBB0_1293
	s_waitcnt vmcnt(7)
	v_mfma_f32_32x32x16_bf16 v[64:79], v[64:67], v[108:111], 0
	s_lshl_b32 s3, s3, 1
	s_add_u32 s3, s28, s3
	s_addc_u32 s8, s29, 0
	s_mul_hi_i32 s9, s2, 0x1400
	s_mulk_i32 s2, 0x1400
	s_add_u32 s46, s18, s2
	s_addc_u32 s9, s19, s9
	s_lshl_b64 s[0:1], s[0:1], 1
	s_add_u32 s2, s3, s0
	s_waitcnt vmcnt(6)
	v_mfma_f32_32x32x16_bf16 v[64:79], v[168:171], v[104:107], v[64:79]
	s_addc_u32 s3, s8, s1
	s_lshl_b32 s0, s34, 1
	s_add_u32 s0, s46, s0
	s_addc_u32 s1, s9, 0
	s_lshl_b32 s8, s37, 7
	s_addk_i32 s8, 0x700
	s_ashr_i32 s9, s8, 31
	s_lshl_b64 s[8:9], s[8:9], 2
	s_add_u32 s8, s35, s8
	s_addc_u32 s9, s36, s9
	s_waitcnt vmcnt(5)
	v_mfma_f32_32x32x16_bf16 v[64:79], v[164:167], v[100:103], v[64:79]
	v_lshlrev_b32_e32 v100, 2, v199
	global_load_dwordx4 v[120:123], v100, s[8:9] offset:144
	global_load_dwordx4 v[124:127], v100, s[8:9] offset:128
	global_load_dwordx4 v[116:119], v100, s[8:9] offset:208
	global_load_dwordx4 v[128:131], v100, s[8:9] offset:192
	v_mov_b32_e32 v199, v177
	v_add_u32_e32 v132, 32, v201
	v_add_u32_e32 v133, 33, v201
	v_add_u32_e32 v134, 34, v201
	s_waitcnt vmcnt(8)
	v_mfma_f32_32x32x16_bf16 v[64:79], v[160:163], v[96:99], v[64:79]
	v_add_u32_e32 v135, 35, v201
	v_add_u32_e32 v136, 36, v201
	v_add_u32_e32 v137, 37, v201
	v_add_u32_e32 v138, 38, v201
	v_add_u32_e32 v139, 39, v201
	v_mov_b32_e32 v203, v177
	s_add_i32 s33, s33, s5
	s_waitcnt vmcnt(7)
	v_mfma_f32_32x32x16_bf16 v[64:79], v[156:159], v[92:95], v[64:79]
	v_lshl_add_u64 v[92:93], s[2:3], 0, v[198:199]
	s_mov_b32 s2, 0x1f000
	v_add_co_u32_e32 v100, vcc, s2, v92
	s_mov_b32 s2, 0x1e000
	s_nop 0
	v_addc_co_u32_e32 v101, vcc, 0, v93, vcc
	s_waitcnt vmcnt(6)
	v_mfma_f32_32x32x16_bf16 v[64:79], v[152:155], v[88:91], v[64:79]
	v_add_co_u32_e32 v102, vcc, s2, v92
	s_cmpk_gt_i32 s33, 0xfff
	s_nop 0
	v_addc_co_u32_e32 v103, vcc, 0, v93, vcc
	v_cmp_gt_u32_e32 vcc, 16, v132
	s_waitcnt vmcnt(5)
	v_mfma_f32_32x32x16_bf16 v[64:79], v[148:151], v[84:87], v[64:79]
	global_load_dwordx4 v[108:111], v[102:103], off offset:1024
	global_load_dwordx4 v[104:107], v[102:103], off offset:2048
	global_load_dwordx4 v[96:99], v[100:101], off
	global_load_dwordx4 v[92:95], v[100:101], off offset:1024
	global_load_dwordx4 v[88:91], v[100:101], off offset:2048
	global_load_dwordx4 v[84:87], v[100:101], off offset:3072
	global_load_dwordx4 v[112:115], v[100:101], off offset:-4096
	s_nop 0
	global_load_dwordx4 v[100:103], v[102:103], off offset:3072
	s_waitcnt vmcnt(12)
	v_mfma_f32_32x32x16_bf16 v[64:79], v[144:147], v[80:83], v[64:79]
	s_waitcnt vmcnt(11)
	v_mov_b32_e32 v80, v122
	s_waitcnt vmcnt(10)
	v_mov_b32_e32 v81, v127
	v_mov_b32_e32 v82, v121
	v_mov_b32_e32 v83, v124
	v_mov_b32_e32 v121, v123
	v_mov_b32_e32 v122, v126
	s_waitcnt vmcnt(8)
	v_mov_b32_e32 v123, v129
	s_nop 1
	v_add_f32_e32 v64, v64, v83
	v_add_f32_e32 v65, v65, v125
	v_cndmask_b32_e32 v64, v222, v64, vcc
	v_cmp_gt_u32_e32 vcc, 16, v133
	v_add_f32_e32 v66, v66, v122
	v_add_f32_e32 v67, v67, v81
	v_cndmask_b32_e32 v65, v222, v65, vcc
	v_cmp_gt_u32_e32 vcc, 16, v134
	v_add_f32_e32 v68, v68, v120
	v_add_f32_e32 v69, v69, v82
	v_cndmask_b32_e32 v66, v222, v66, vcc
	v_cmp_gt_u32_e32 vcc, 16, v135
	v_add_f32_e32 v70, v70, v80
	v_mov_b32_e32 v124, v131
	v_cndmask_b32_e32 v67, v222, v67, vcc
	v_cmp_gt_u32_e32 vcc, 16, v136
	v_mov_b32_e32 v126, v128
	v_add_f32_e32 v71, v71, v121
	v_cndmask_b32_e32 v68, v222, v68, vcc
	v_cmp_gt_u32_e32 vcc, 16, v137
	v_add_u32_e32 v80, 49, v201
	v_add_f32_e32 v72, v72, v126
	v_cndmask_b32_e32 v69, v222, v69, vcc
	v_cmp_gt_u32_e32 vcc, 16, v138
	v_add_f32_e32 v73, v73, v123
	v_add_f32_e32 v74, v74, v130
	v_cndmask_b32_e32 v70, v222, v70, vcc
	v_cmp_gt_u32_e32 vcc, 16, v139
	v_add_f32_e32 v75, v75, v124
	v_add_f32_e32 v76, v76, v116
	v_cndmask_b32_e32 v71, v222, v71, vcc
	v_cmp_lt_u32_e32 vcc, 48, v132
	v_add_f32_e32 v77, v77, v117
	v_add_f32_e32 v78, v78, v118
	v_cndmask_b32_e32 v72, v222, v72, vcc
	v_cmp_gt_u32_e32 vcc, 16, v80
	v_add_u32_e32 v80, 50, v201
	v_add_f32_e32 v79, v79, v119
	v_cndmask_b32_e32 v73, v222, v73, vcc
	v_cmp_gt_u32_e32 vcc, 16, v80
	v_add_u32_e32 v80, 51, v201
	v_mbcnt_lo_u32_b32 v81, -1, 0
	v_mbcnt_hi_u32_b32 v81, -1, v81
	s_nop 0
	v_cndmask_b32_e32 v74, v222, v74, vcc
	v_cmp_gt_u32_e32 vcc, 16, v80
	v_add_u32_e32 v80, 52, v201
	v_lshlrev_b32_e32 v81, 2, v81
	v_cndmask_b32_e32 v75, v222, v75, vcc
	v_cmp_gt_u32_e32 vcc, 16, v80
	v_add_u32_e32 v80, 53, v201
	v_xor_b32_e32 v81, 0x80, v81
	v_cndmask_b32_e32 v76, v222, v76, vcc
	v_cmp_gt_u32_e32 vcc, 16, v80
	v_add_u32_e32 v80, 54, v201
	s_nop 0
	v_cndmask_b32_e32 v77, v222, v77, vcc
	v_cmp_gt_u32_e32 vcc, 16, v80
	v_add_u32_e32 v80, 55, v201
	v_mov_b32_e32 v201, v177
	v_cndmask_b32_e32 v78, v222, v78, vcc
	v_cmp_gt_u32_e32 vcc, 16, v80
	v_max3_f32 v80, v64, s11, v65
	v_max3_f32 v80, v80, v66, v67
	v_max3_f32 v80, v80, v68, v69
	v_max3_f32 v80, v80, v70, v71
	v_max3_f32 v80, v80, v72, v73
	v_max3_f32 v80, v80, v74, v75
	v_cndmask_b32_e32 v79, v222, v79, vcc
	v_max3_f32 v80, v80, v76, v77
	v_max3_f32 v80, v80, v78, v79
	ds_bpermute_b32 v81, v81, v80
	s_waitcnt lgkmcnt(0)
	v_max3_f32 v80, v206, v80, v81
	v_sub_f32_e32 v64, v64, v80
	v_exp_f32_e32 v82, v64
	v_sub_f32_e32 v64, v65, v80
	v_exp_f32_e32 v65, v64
	v_sub_f32_e32 v64, v66, v80
	v_exp_f32_e32 v83, v64
	v_sub_f32_e32 v64, v67, v80
	v_exp_f32_e32 v116, v64
	v_sub_f32_e32 v64, v68, v80
	v_exp_f32_e32 v117, v64
	v_sub_f32_e32 v64, v69, v80
	v_exp_f32_e32 v118, v64
	v_sub_f32_e32 v64, v70, v80
	v_exp_f32_e32 v119, v64
	v_sub_f32_e32 v64, v71, v80
	v_exp_f32_e32 v120, v64
	v_sub_f32_e32 v64, v72, v80
	v_exp_f32_e32 v121, v64
	v_sub_f32_e32 v64, v73, v80
	v_exp_f32_e32 v122, v64
	v_sub_f32_e32 v64, v74, v80
	v_exp_f32_e32 v74, v64
	v_sub_f32_e32 v64, v75, v80
	v_exp_f32_e32 v75, v64
	v_sub_f32_e32 v64, v76, v80
	v_sub_f32_e32 v66, v78, v80
	v_sub_f32_e32 v81, v206, v80
	v_exp_f32_e32 v76, v64
	v_sub_f32_e32 v64, v77, v80
	v_exp_f32_e32 v78, v66
	v_sub_f32_e32 v66, v79, v80
	v_bfe_u32 v68, v116, 16, 1
	v_bfe_u32 v69, v65, 16, 1
	v_exp_f32_e32 v77, v64
	v_exp_f32_e32 v64, v81
	v_exp_f32_e32 v79, v66
	v_add3_u32 v70, v65, v69, s25
	v_add3_u32 v71, v116, v68, s25
	v_bfe_u32 v68, v82, 16, 1
	v_bfe_u32 v69, v83, 16, 1
	v_bfe_u32 v72, v117, 16, 1
	v_bfe_u32 v73, v119, 16, 1
	v_bfe_u32 v66, v120, 16, 1
	v_bfe_u32 v67, v118, 16, 1
	v_add3_u32 v73, v119, v73, s25
	v_add3_u32 v72, v117, v72, s25
	v_add3_u32 v69, v83, v69, s25
	v_add3_u32 v68, v82, v68, s25
	v_add3_u32 v67, v118, v67, s25
	v_add3_u32 v66, v120, v66, s25
	v_lshrrev_b32_e32 v80, 16, v68
	v_lshrrev_b32_e32 v81, 16, v69
	v_lshrrev_b32_e32 v68, 16, v72
	v_lshrrev_b32_e32 v69, 16, v73
	v_bfe_u32 v72, v75, 16, 1
	v_bfe_u32 v73, v122, 16, 1
	v_and_or_b32 v69, v66, s10, v69
	v_and_or_b32 v68, v67, s10, v68
	v_and_or_b32 v67, v71, s10, v81
	v_and_or_b32 v66, v70, s10, v80
	v_add3_u32 v80, v122, v73, s25
	v_add3_u32 v81, v75, v72, s25
	v_bfe_u32 v72, v121, 16, 1
	v_bfe_u32 v73, v74, 16, 1
	v_bfe_u32 v124, v78, 16, 1
	v_pk_mul_f32 v[62:63], v[62:63], v[64:65] op_sel_hi:[1,0]
	v_pk_mul_f32 v[60:61], v[60:61], v[64:65] op_sel_hi:[1,0]
	v_pk_mul_f32 v[58:59], v[58:59], v[64:65] op_sel_hi:[1,0]
	v_pk_mul_f32 v[56:57], v[56:57], v[64:65] op_sel_hi:[1,0]
	v_pk_mul_f32 v[54:55], v[54:55], v[64:65] op_sel_hi:[1,0]
	v_pk_mul_f32 v[52:53], v[52:53], v[64:65] op_sel_hi:[1,0]
	v_pk_mul_f32 v[50:51], v[50:51], v[64:65] op_sel_hi:[1,0]
	v_pk_mul_f32 v[48:49], v[48:49], v[64:65] op_sel_hi:[1,0]
	v_bfe_u32 v70, v79, 16, 1
	v_add3_u32 v124, v78, v124, s25
	v_add3_u32 v73, v74, v73, s25
	v_add3_u32 v72, v121, v72, s25
	v_add3_u32 v70, v79, v70, s25
	v_lshrrev_b32_e32 v125, 16, v72
	s_waitcnt vmcnt(1)
	v_mfma_f32_32x32x16_bf16 v[48:63], v[112:115], v[66:69], v[48:63]
	v_lshrrev_b32_e32 v112, 16, v73
	v_lshrrev_b32_e32 v73, 16, v124
	v_and_or_b32 v73, v70, s10, v73
	v_and_or_b32 v70, v80, s10, v125
	v_add_f32_e32 v80, 0, v82
	v_pk_mul_f32 v[46:47], v[46:47], v[64:65] op_sel_hi:[1,0]
	v_pk_mul_f32 v[44:45], v[44:45], v[64:65] op_sel_hi:[1,0]
	v_pk_mul_f32 v[42:43], v[42:43], v[64:65] op_sel_hi:[1,0]
	v_pk_mul_f32 v[40:41], v[40:41], v[64:65] op_sel_hi:[1,0]
	v_pk_mul_f32 v[38:39], v[38:39], v[64:65] op_sel_hi:[1,0]
	v_pk_mul_f32 v[36:37], v[36:37], v[64:65] op_sel_hi:[1,0]
	v_pk_mul_f32 v[34:35], v[34:35], v[64:65] op_sel_hi:[1,0]
	v_pk_mul_f32 v[32:33], v[32:33], v[64:65] op_sel_hi:[1,0]
	v_pk_mul_f32 v[30:31], v[30:31], v[64:65] op_sel_hi:[1,0]
	v_pk_mul_f32 v[28:29], v[28:29], v[64:65] op_sel_hi:[1,0]
	v_pk_mul_f32 v[26:27], v[26:27], v[64:65] op_sel_hi:[1,0]
	v_pk_mul_f32 v[24:25], v[24:25], v[64:65] op_sel_hi:[1,0]
	v_pk_mul_f32 v[22:23], v[22:23], v[64:65] op_sel_hi:[1,0]
	v_pk_mul_f32 v[20:21], v[20:21], v[64:65] op_sel_hi:[1,0]
	v_pk_mul_f32 v[18:19], v[18:19], v[64:65] op_sel_hi:[1,0]
	v_pk_mul_f32 v[16:17], v[16:17], v[64:65] op_sel_hi:[1,0]
	v_pk_mul_f32 v[14:15], v[14:15], v[64:65] op_sel_hi:[1,0]
	v_pk_mul_f32 v[12:13], v[12:13], v[64:65] op_sel_hi:[1,0]
	v_pk_mul_f32 v[10:11], v[10:11], v[64:65] op_sel_hi:[1,0]
	v_pk_mul_f32 v[8:9], v[8:9], v[64:65] op_sel_hi:[1,0]
	v_pk_mul_f32 v[6:7], v[6:7], v[64:65] op_sel_hi:[1,0]
	v_pk_mul_f32 v[4:5], v[4:5], v[64:65] op_sel_hi:[1,0]
	v_pk_mul_f32 v[2:3], v[2:3], v[64:65] op_sel_hi:[1,0]
	v_pk_mul_f32 v[0:1], v[0:1], v[64:65] op_sel_hi:[1,0]
	v_add_f32_e32 v65, v65, v80
	v_add_f32_e32 v65, v83, v65
	v_add_f32_e32 v65, v116, v65
	v_add_f32_e32 v65, v117, v65
	v_add_f32_e32 v65, v118, v65
	v_add_f32_e32 v65, v119, v65
	v_add_f32_e32 v65, v120, v65
	v_add_f32_e32 v65, v121, v65
	v_add_f32_e32 v65, v122, v65
	v_add_f32_e32 v65, v74, v65
	v_add_f32_e32 v65, v75, v65
	v_add_f32_e32 v65, v76, v65
	v_add_f32_e32 v65, v77, v65
	v_add_f32_e32 v65, v78, v65
	v_add_f32_e32 v65, v79, v65
	v_fmac_f32_e32 v65, v207, v64
	v_mbcnt_lo_u32_b32 v64, -1, 0
	v_mbcnt_hi_u32_b32 v64, -1, v64
	v_bfe_u32 v123, v76, 16, 1
	v_lshlrev_b32_e32 v64, 2, v64
	v_xor_b32_e32 v64, 0x80, v64
	ds_bpermute_b32 v64, v64, v65
	v_bfe_u32 v71, v77, 16, 1
	v_add3_u32 v123, v76, v123, s25
	v_mfma_f32_32x32x16_bf16 v[32:47], v[104:107], v[66:69], v[32:47]
	v_add3_u32 v71, v77, v71, s25
	s_waitcnt lgkmcnt(0)
	v_add_f32_e32 v64, v65, v64
	v_div_scale_f32 v65, s[2:3], v64, v64, 1.0
	v_lshrrev_b32_e32 v72, 16, v123
	v_and_or_b32 v72, v71, s10, v72
	v_and_or_b32 v71, v81, s10, v112
	v_mfma_f32_32x32x16_bf16 v[16:31], v[96:99], v[66:69], v[16:31]
	v_mfma_f32_32x32x16_bf16 v[0:15], v[88:91], v[66:69], v[0:15]
	v_rcp_f32_e32 v66, v65
	s_nop 0
	v_fma_f32 v67, -v65, v66, 1.0
	v_fmac_f32_e32 v66, v67, v66
	v_div_scale_f32 v67, vcc, 1.0, v64, 1.0
	v_mfma_f32_32x32x16_bf16 v[48:63], v[108:111], v[70:73], v[48:63]
	v_mul_f32_e32 v68, v67, v66
	v_fma_f32 v69, -v65, v68, v67
	v_fmac_f32_e32 v68, v69, v66
	v_fma_f32 v65, -v65, v68, v67
	v_div_fmas_f32 v65, v65, v66, v68
	v_div_fixup_f32 v66, v65, v64, 1.0
	v_lshl_add_u64 v[64:65], s[0:1], 0, v[200:201]
	s_nop 4
	v_mov_b32_e32 v68, v48
	v_mov_b32_e32 v69, v50
	v_pk_mul_f32 v[68:69], v[68:69], v[66:67] op_sel_hi:[1,0]
	v_mov_b32_e32 v50, v49
	v_pk_mul_f32 v[48:49], v[50:51], v[66:67] op_sel_hi:[1,0]
	v_and_b32_sdwa v51, v68, v231 dst_sel:DWORD dst_unused:UNUSED_PAD src0_sel:WORD_1 src1_sel:DWORD
	v_add3_u32 v51, v68, v51, s25
	v_and_b32_sdwa v67, v49, v231 dst_sel:DWORD dst_unused:UNUSED_PAD src0_sel:WORD_1 src1_sel:DWORD
	v_and_b32_sdwa v68, v48, v231 dst_sel:DWORD dst_unused:UNUSED_PAD src0_sel:WORD_1 src1_sel:DWORD
	v_and_b32_sdwa v50, v69, v231 dst_sel:DWORD dst_unused:UNUSED_PAD src0_sel:WORD_1 src1_sel:DWORD
	v_add3_u32 v49, v49, v67, s25
	v_add3_u32 v48, v48, v68, s25
	v_add3_u32 v50, v69, v50, s25
	v_and_b32_e32 v49, 0xffff0000, v49
	v_and_b32_e32 v48, 0xffff0000, v48
	v_lshl_add_u64 v[64:65], v[64:65], 0, v[202:203]
	v_or_b32_sdwa v49, v49, v50 dst_sel:DWORD dst_unused:UNUSED_PAD src0_sel:DWORD src1_sel:WORD_1
	v_or_b32_sdwa v48, v48, v51 dst_sel:DWORD dst_unused:UNUSED_PAD src0_sel:DWORD src1_sel:WORD_1
	global_store_dwordx2 v[64:65], v[48:49], off
	v_mov_b32_e32 v48, v52
	v_mov_b32_e32 v49, v54
	v_pk_mul_f32 v[48:49], v[48:49], v[66:67] op_sel_hi:[1,0]
	v_mov_b32_e32 v54, v53
	v_pk_mul_f32 v[50:51], v[54:55], v[66:67] op_sel_hi:[1,0]
	v_and_b32_sdwa v52, v49, v231 dst_sel:DWORD dst_unused:UNUSED_PAD src0_sel:WORD_1 src1_sel:DWORD
	v_and_b32_sdwa v53, v48, v231 dst_sel:DWORD dst_unused:UNUSED_PAD src0_sel:WORD_1 src1_sel:DWORD
	v_add3_u32 v48, v48, v53, s25
	v_add3_u32 v49, v49, v52, s25
	v_and_b32_sdwa v52, v51, v231 dst_sel:DWORD dst_unused:UNUSED_PAD src0_sel:WORD_1 src1_sel:DWORD
	v_and_b32_sdwa v53, v50, v231 dst_sel:DWORD dst_unused:UNUSED_PAD src0_sel:WORD_1 src1_sel:DWORD
	v_add3_u32 v51, v51, v52, s25
	v_add3_u32 v50, v50, v53, s25
	v_and_b32_e32 v51, 0xffff0000, v51
	v_and_b32_e32 v50, 0xffff0000, v50
	v_or_b32_sdwa v49, v51, v49 dst_sel:DWORD dst_unused:UNUSED_PAD src0_sel:DWORD src1_sel:WORD_1
	v_or_b32_sdwa v48, v50, v48 dst_sel:DWORD dst_unused:UNUSED_PAD src0_sel:DWORD src1_sel:WORD_1
	global_store_dwordx2 v[64:65], v[48:49], off offset:16
	v_mov_b32_e32 v48, v56
	v_mov_b32_e32 v49, v58
	v_pk_mul_f32 v[48:49], v[48:49], v[66:67] op_sel_hi:[1,0]
	v_mov_b32_e32 v58, v57
	v_pk_mul_f32 v[50:51], v[58:59], v[66:67] op_sel_hi:[1,0]
	v_and_b32_sdwa v52, v49, v231 dst_sel:DWORD dst_unused:UNUSED_PAD src0_sel:WORD_1 src1_sel:DWORD
	v_and_b32_sdwa v53, v48, v231 dst_sel:DWORD dst_unused:UNUSED_PAD src0_sel:WORD_1 src1_sel:DWORD
	v_add3_u32 v48, v48, v53, s25
	v_add3_u32 v49, v49, v52, s25
	v_and_b32_sdwa v52, v51, v231 dst_sel:DWORD dst_unused:UNUSED_PAD src0_sel:WORD_1 src1_sel:DWORD
	v_and_b32_sdwa v53, v50, v231 dst_sel:DWORD dst_unused:UNUSED_PAD src0_sel:WORD_1 src1_sel:DWORD
	v_add3_u32 v51, v51, v52, s25
	v_add3_u32 v50, v50, v53, s25
	v_and_b32_e32 v51, 0xffff0000, v51
	v_and_b32_e32 v50, 0xffff0000, v50
	s_waitcnt vmcnt(2)
	v_mfma_f32_32x32x16_bf16 v[32:47], v[100:103], v[70:73], v[32:47]
	v_or_b32_sdwa v49, v51, v49 dst_sel:DWORD dst_unused:UNUSED_PAD src0_sel:DWORD src1_sel:WORD_1
	v_or_b32_sdwa v48, v50, v48 dst_sel:DWORD dst_unused:UNUSED_PAD src0_sel:DWORD src1_sel:WORD_1
	global_store_dwordx2 v[64:65], v[48:49], off offset:32
	v_mov_b32_e32 v48, v60
	v_mov_b32_e32 v49, v62
	v_pk_mul_f32 v[48:49], v[48:49], v[66:67] op_sel_hi:[1,0]
	v_mov_b32_e32 v62, v61
	v_pk_mul_f32 v[50:51], v[62:63], v[66:67] op_sel_hi:[1,0]
	v_and_b32_sdwa v52, v49, v231 dst_sel:DWORD dst_unused:UNUSED_PAD src0_sel:WORD_1 src1_sel:DWORD
	v_and_b32_sdwa v53, v48, v231 dst_sel:DWORD dst_unused:UNUSED_PAD src0_sel:WORD_1 src1_sel:DWORD
	v_add3_u32 v48, v48, v53, s25
	v_add3_u32 v49, v49, v52, s25
	v_and_b32_sdwa v52, v51, v231 dst_sel:DWORD dst_unused:UNUSED_PAD src0_sel:WORD_1 src1_sel:DWORD
	v_and_b32_sdwa v53, v50, v231 dst_sel:DWORD dst_unused:UNUSED_PAD src0_sel:WORD_1 src1_sel:DWORD
	v_add3_u32 v51, v51, v52, s25
	v_add3_u32 v50, v50, v53, s25
	v_and_b32_e32 v51, 0xffff0000, v51
	v_and_b32_e32 v50, 0xffff0000, v50
	v_or_b32_sdwa v49, v51, v49 dst_sel:DWORD dst_unused:UNUSED_PAD src0_sel:DWORD src1_sel:WORD_1
	v_or_b32_sdwa v48, v50, v48 dst_sel:DWORD dst_unused:UNUSED_PAD src0_sel:DWORD src1_sel:WORD_1
	global_store_dwordx2 v[64:65], v[48:49], off offset:48
	v_mov_b32_e32 v48, v32
	v_mov_b32_e32 v49, v34
	v_pk_mul_f32 v[48:49], v[48:49], v[66:67] op_sel_hi:[1,0]
	v_mov_b32_e32 v34, v33
	v_pk_mul_f32 v[32:33], v[34:35], v[66:67] op_sel_hi:[1,0]
	v_and_b32_sdwa v34, v49, v231 dst_sel:DWORD dst_unused:UNUSED_PAD src0_sel:WORD_1 src1_sel:DWORD
	v_and_b32_sdwa v35, v48, v231 dst_sel:DWORD dst_unused:UNUSED_PAD src0_sel:WORD_1 src1_sel:DWORD
	v_add3_u32 v35, v48, v35, s25
	v_add3_u32 v34, v49, v34, s25
	v_and_b32_sdwa v48, v33, v231 dst_sel:DWORD dst_unused:UNUSED_PAD src0_sel:WORD_1 src1_sel:DWORD
	v_and_b32_sdwa v49, v32, v231 dst_sel:DWORD dst_unused:UNUSED_PAD src0_sel:WORD_1 src1_sel:DWORD
	v_add3_u32 v33, v33, v48, s25
	v_add3_u32 v32, v32, v49, s25
	v_and_b32_e32 v33, 0xffff0000, v33
	v_and_b32_e32 v32, 0xffff0000, v32
	v_or_b32_sdwa v33, v33, v34 dst_sel:DWORD dst_unused:UNUSED_PAD src0_sel:DWORD src1_sel:WORD_1
	v_or_b32_sdwa v32, v32, v35 dst_sel:DWORD dst_unused:UNUSED_PAD src0_sel:DWORD src1_sel:WORD_1
	global_store_dwordx2 v[64:65], v[32:33], off offset:64
	v_mov_b32_e32 v32, v36
	v_mov_b32_e32 v33, v38
	v_pk_mul_f32 v[32:33], v[32:33], v[66:67] op_sel_hi:[1,0]
	v_mov_b32_e32 v38, v37
	v_pk_mul_f32 v[34:35], v[38:39], v[66:67] op_sel_hi:[1,0]
	v_and_b32_sdwa v36, v33, v231 dst_sel:DWORD dst_unused:UNUSED_PAD src0_sel:WORD_1 src1_sel:DWORD
	v_and_b32_sdwa v37, v32, v231 dst_sel:DWORD dst_unused:UNUSED_PAD src0_sel:WORD_1 src1_sel:DWORD
	v_add3_u32 v32, v32, v37, s25
	v_add3_u32 v33, v33, v36, s25
	v_and_b32_sdwa v36, v35, v231 dst_sel:DWORD dst_unused:UNUSED_PAD src0_sel:WORD_1 src1_sel:DWORD
	v_and_b32_sdwa v37, v34, v231 dst_sel:DWORD dst_unused:UNUSED_PAD src0_sel:WORD_1 src1_sel:DWORD
	v_add3_u32 v35, v35, v36, s25
	v_add3_u32 v34, v34, v37, s25
	v_and_b32_e32 v35, 0xffff0000, v35
	v_and_b32_e32 v34, 0xffff0000, v34
	v_or_b32_sdwa v33, v35, v33 dst_sel:DWORD dst_unused:UNUSED_PAD src0_sel:DWORD src1_sel:WORD_1
	v_or_b32_sdwa v32, v34, v32 dst_sel:DWORD dst_unused:UNUSED_PAD src0_sel:DWORD src1_sel:WORD_1
	global_store_dwordx2 v[64:65], v[32:33], off offset:80
	v_mov_b32_e32 v32, v40
	v_mov_b32_e32 v33, v42
	v_pk_mul_f32 v[32:33], v[32:33], v[66:67] op_sel_hi:[1,0]
	v_mov_b32_e32 v42, v41
	v_pk_mul_f32 v[34:35], v[42:43], v[66:67] op_sel_hi:[1,0]
	v_and_b32_sdwa v36, v33, v231 dst_sel:DWORD dst_unused:UNUSED_PAD src0_sel:WORD_1 src1_sel:DWORD
	v_and_b32_sdwa v37, v32, v231 dst_sel:DWORD dst_unused:UNUSED_PAD src0_sel:WORD_1 src1_sel:DWORD
	v_add3_u32 v32, v32, v37, s25
	v_add3_u32 v33, v33, v36, s25
	v_and_b32_sdwa v36, v35, v231 dst_sel:DWORD dst_unused:UNUSED_PAD src0_sel:WORD_1 src1_sel:DWORD
	v_and_b32_sdwa v37, v34, v231 dst_sel:DWORD dst_unused:UNUSED_PAD src0_sel:WORD_1 src1_sel:DWORD
	v_add3_u32 v35, v35, v36, s25
	v_add3_u32 v34, v34, v37, s25
	v_and_b32_e32 v35, 0xffff0000, v35
	v_and_b32_e32 v34, 0xffff0000, v34
	v_mfma_f32_32x32x16_bf16 v[16:31], v[92:95], v[70:73], v[16:31]
	v_or_b32_sdwa v33, v35, v33 dst_sel:DWORD dst_unused:UNUSED_PAD src0_sel:DWORD src1_sel:WORD_1
	v_or_b32_sdwa v32, v34, v32 dst_sel:DWORD dst_unused:UNUSED_PAD src0_sel:DWORD src1_sel:WORD_1
	global_store_dwordx2 v[64:65], v[32:33], off offset:96
	v_mov_b32_e32 v32, v44
	v_mov_b32_e32 v33, v46
	v_pk_mul_f32 v[32:33], v[32:33], v[66:67] op_sel_hi:[1,0]
	v_mov_b32_e32 v46, v45
	v_pk_mul_f32 v[34:35], v[46:47], v[66:67] op_sel_hi:[1,0]
	v_and_b32_sdwa v36, v33, v231 dst_sel:DWORD dst_unused:UNUSED_PAD src0_sel:WORD_1 src1_sel:DWORD
	v_and_b32_sdwa v37, v32, v231 dst_sel:DWORD dst_unused:UNUSED_PAD src0_sel:WORD_1 src1_sel:DWORD
	v_add3_u32 v32, v32, v37, s25
	v_add3_u32 v33, v33, v36, s25
	v_and_b32_sdwa v36, v35, v231 dst_sel:DWORD dst_unused:UNUSED_PAD src0_sel:WORD_1 src1_sel:DWORD
	v_and_b32_sdwa v37, v34, v231 dst_sel:DWORD dst_unused:UNUSED_PAD src0_sel:WORD_1 src1_sel:DWORD
	v_add3_u32 v35, v35, v36, s25
	v_add3_u32 v34, v34, v37, s25
	v_and_b32_e32 v35, 0xffff0000, v35
	v_and_b32_e32 v34, 0xffff0000, v34
	v_or_b32_sdwa v33, v35, v33 dst_sel:DWORD dst_unused:UNUSED_PAD src0_sel:DWORD src1_sel:WORD_1
	v_or_b32_sdwa v32, v34, v32 dst_sel:DWORD dst_unused:UNUSED_PAD src0_sel:DWORD src1_sel:WORD_1
	global_store_dwordx2 v[64:65], v[32:33], off offset:112
	v_mov_b32_e32 v32, v16
	v_mov_b32_e32 v33, v18
	v_pk_mul_f32 v[32:33], v[32:33], v[66:67] op_sel_hi:[1,0]
	v_mov_b32_e32 v18, v17
	v_pk_mul_f32 v[16:17], v[18:19], v[66:67] op_sel_hi:[1,0]
	v_and_b32_sdwa v18, v33, v231 dst_sel:DWORD dst_unused:UNUSED_PAD src0_sel:WORD_1 src1_sel:DWORD
	v_and_b32_sdwa v19, v32, v231 dst_sel:DWORD dst_unused:UNUSED_PAD src0_sel:WORD_1 src1_sel:DWORD
	v_add3_u32 v19, v32, v19, s25
	v_add3_u32 v18, v33, v18, s25
	v_and_b32_sdwa v32, v17, v231 dst_sel:DWORD dst_unused:UNUSED_PAD src0_sel:WORD_1 src1_sel:DWORD
	v_and_b32_sdwa v33, v16, v231 dst_sel:DWORD dst_unused:UNUSED_PAD src0_sel:WORD_1 src1_sel:DWORD
	v_add3_u32 v17, v17, v32, s25
	v_add3_u32 v16, v16, v33, s25
	v_and_b32_e32 v17, 0xffff0000, v17
	v_and_b32_e32 v16, 0xffff0000, v16
	v_or_b32_sdwa v17, v17, v18 dst_sel:DWORD dst_unused:UNUSED_PAD src0_sel:DWORD src1_sel:WORD_1
	v_or_b32_sdwa v16, v16, v19 dst_sel:DWORD dst_unused:UNUSED_PAD src0_sel:DWORD src1_sel:WORD_1
	global_store_dwordx2 v[64:65], v[16:17], off offset:128
	v_mov_b32_e32 v16, v20
	v_mov_b32_e32 v17, v22
	v_pk_mul_f32 v[16:17], v[16:17], v[66:67] op_sel_hi:[1,0]
	v_mov_b32_e32 v22, v21
	v_pk_mul_f32 v[18:19], v[22:23], v[66:67] op_sel_hi:[1,0]
	v_and_b32_sdwa v20, v17, v231 dst_sel:DWORD dst_unused:UNUSED_PAD src0_sel:WORD_1 src1_sel:DWORD
	v_and_b32_sdwa v21, v16, v231 dst_sel:DWORD dst_unused:UNUSED_PAD src0_sel:WORD_1 src1_sel:DWORD
	v_add3_u32 v16, v16, v21, s25
	v_add3_u32 v17, v17, v20, s25
	v_and_b32_sdwa v20, v19, v231 dst_sel:DWORD dst_unused:UNUSED_PAD src0_sel:WORD_1 src1_sel:DWORD
	v_and_b32_sdwa v21, v18, v231 dst_sel:DWORD dst_unused:UNUSED_PAD src0_sel:WORD_1 src1_sel:DWORD
	v_add3_u32 v19, v19, v20, s25
	v_add3_u32 v18, v18, v21, s25
	v_and_b32_e32 v19, 0xffff0000, v19
	v_and_b32_e32 v18, 0xffff0000, v18
	v_or_b32_sdwa v17, v19, v17 dst_sel:DWORD dst_unused:UNUSED_PAD src0_sel:DWORD src1_sel:WORD_1
	v_or_b32_sdwa v16, v18, v16 dst_sel:DWORD dst_unused:UNUSED_PAD src0_sel:DWORD src1_sel:WORD_1
	global_store_dwordx2 v[64:65], v[16:17], off offset:144
	v_mov_b32_e32 v16, v24
	v_mov_b32_e32 v17, v26
	v_pk_mul_f32 v[16:17], v[16:17], v[66:67] op_sel_hi:[1,0]
	v_mov_b32_e32 v26, v25
	v_pk_mul_f32 v[18:19], v[26:27], v[66:67] op_sel_hi:[1,0]
	v_and_b32_sdwa v20, v17, v231 dst_sel:DWORD dst_unused:UNUSED_PAD src0_sel:WORD_1 src1_sel:DWORD
	v_and_b32_sdwa v21, v16, v231 dst_sel:DWORD dst_unused:UNUSED_PAD src0_sel:WORD_1 src1_sel:DWORD
	v_add3_u32 v16, v16, v21, s25
	v_add3_u32 v17, v17, v20, s25
	v_and_b32_sdwa v20, v19, v231 dst_sel:DWORD dst_unused:UNUSED_PAD src0_sel:WORD_1 src1_sel:DWORD
	v_and_b32_sdwa v21, v18, v231 dst_sel:DWORD dst_unused:UNUSED_PAD src0_sel:WORD_1 src1_sel:DWORD
	v_add3_u32 v19, v19, v20, s25
	v_add3_u32 v18, v18, v21, s25
	v_and_b32_e32 v19, 0xffff0000, v19
	v_and_b32_e32 v18, 0xffff0000, v18
	v_mfma_f32_32x32x16_bf16 v[0:15], v[84:87], v[70:73], v[0:15]
	v_or_b32_sdwa v17, v19, v17 dst_sel:DWORD dst_unused:UNUSED_PAD src0_sel:DWORD src1_sel:WORD_1
	v_or_b32_sdwa v16, v18, v16 dst_sel:DWORD dst_unused:UNUSED_PAD src0_sel:DWORD src1_sel:WORD_1
	global_store_dwordx2 v[64:65], v[16:17], off offset:160
	v_mov_b32_e32 v16, v28
	v_mov_b32_e32 v17, v30
	v_pk_mul_f32 v[16:17], v[16:17], v[66:67] op_sel_hi:[1,0]
	v_mov_b32_e32 v30, v29
	v_pk_mul_f32 v[18:19], v[30:31], v[66:67] op_sel_hi:[1,0]
	v_and_b32_sdwa v20, v17, v231 dst_sel:DWORD dst_unused:UNUSED_PAD src0_sel:WORD_1 src1_sel:DWORD
	v_and_b32_sdwa v21, v16, v231 dst_sel:DWORD dst_unused:UNUSED_PAD src0_sel:WORD_1 src1_sel:DWORD
	v_add3_u32 v16, v16, v21, s25
	v_add3_u32 v17, v17, v20, s25
	v_and_b32_sdwa v20, v19, v231 dst_sel:DWORD dst_unused:UNUSED_PAD src0_sel:WORD_1 src1_sel:DWORD
	v_and_b32_sdwa v21, v18, v231 dst_sel:DWORD dst_unused:UNUSED_PAD src0_sel:WORD_1 src1_sel:DWORD
	v_add3_u32 v19, v19, v20, s25
	v_add3_u32 v18, v18, v21, s25
	v_and_b32_e32 v19, 0xffff0000, v19
	v_and_b32_e32 v18, 0xffff0000, v18
	v_or_b32_sdwa v17, v19, v17 dst_sel:DWORD dst_unused:UNUSED_PAD src0_sel:DWORD src1_sel:WORD_1
	v_or_b32_sdwa v16, v18, v16 dst_sel:DWORD dst_unused:UNUSED_PAD src0_sel:DWORD src1_sel:WORD_1
	global_store_dwordx2 v[64:65], v[16:17], off offset:176
	v_mov_b32_e32 v16, v0
	v_mov_b32_e32 v17, v2
	v_pk_mul_f32 v[16:17], v[16:17], v[66:67] op_sel_hi:[1,0]
	v_mov_b32_e32 v2, v1
	v_pk_mul_f32 v[0:1], v[2:3], v[66:67] op_sel_hi:[1,0]
	v_and_b32_sdwa v2, v17, v231 dst_sel:DWORD dst_unused:UNUSED_PAD src0_sel:WORD_1 src1_sel:DWORD
	v_and_b32_sdwa v3, v16, v231 dst_sel:DWORD dst_unused:UNUSED_PAD src0_sel:WORD_1 src1_sel:DWORD
	v_add3_u32 v3, v16, v3, s25
	v_add3_u32 v2, v17, v2, s25
	v_and_b32_sdwa v16, v1, v231 dst_sel:DWORD dst_unused:UNUSED_PAD src0_sel:WORD_1 src1_sel:DWORD
	v_and_b32_sdwa v17, v0, v231 dst_sel:DWORD dst_unused:UNUSED_PAD src0_sel:WORD_1 src1_sel:DWORD
	v_add3_u32 v1, v1, v16, s25
	v_add3_u32 v0, v0, v17, s25
	v_and_b32_e32 v1, 0xffff0000, v1
	v_and_b32_e32 v0, 0xffff0000, v0
	v_or_b32_sdwa v1, v1, v2 dst_sel:DWORD dst_unused:UNUSED_PAD src0_sel:DWORD src1_sel:WORD_1
	v_or_b32_sdwa v0, v0, v3 dst_sel:DWORD dst_unused:UNUSED_PAD src0_sel:DWORD src1_sel:WORD_1
	global_store_dwordx2 v[64:65], v[0:1], off offset:192
	v_mov_b32_e32 v0, v4
	v_mov_b32_e32 v1, v6
	v_pk_mul_f32 v[0:1], v[0:1], v[66:67] op_sel_hi:[1,0]
	v_mov_b32_e32 v6, v5
	v_pk_mul_f32 v[2:3], v[6:7], v[66:67] op_sel_hi:[1,0]
	v_and_b32_sdwa v4, v1, v231 dst_sel:DWORD dst_unused:UNUSED_PAD src0_sel:WORD_1 src1_sel:DWORD
	v_and_b32_sdwa v5, v0, v231 dst_sel:DWORD dst_unused:UNUSED_PAD src0_sel:WORD_1 src1_sel:DWORD
	v_add3_u32 v0, v0, v5, s25
	v_add3_u32 v1, v1, v4, s25
	v_and_b32_sdwa v4, v3, v231 dst_sel:DWORD dst_unused:UNUSED_PAD src0_sel:WORD_1 src1_sel:DWORD
	v_and_b32_sdwa v5, v2, v231 dst_sel:DWORD dst_unused:UNUSED_PAD src0_sel:WORD_1 src1_sel:DWORD
	v_add3_u32 v3, v3, v4, s25
	v_add3_u32 v2, v2, v5, s25
	v_and_b32_e32 v3, 0xffff0000, v3
	v_and_b32_e32 v2, 0xffff0000, v2
	v_or_b32_sdwa v1, v3, v1 dst_sel:DWORD dst_unused:UNUSED_PAD src0_sel:DWORD src1_sel:WORD_1
	v_or_b32_sdwa v0, v2, v0 dst_sel:DWORD dst_unused:UNUSED_PAD src0_sel:DWORD src1_sel:WORD_1
	global_store_dwordx2 v[64:65], v[0:1], off offset:208
	v_mov_b32_e32 v0, v8
	v_mov_b32_e32 v1, v10
	v_pk_mul_f32 v[0:1], v[0:1], v[66:67] op_sel_hi:[1,0]
	v_mov_b32_e32 v10, v9
	v_pk_mul_f32 v[2:3], v[10:11], v[66:67] op_sel_hi:[1,0]
	v_and_b32_sdwa v4, v1, v231 dst_sel:DWORD dst_unused:UNUSED_PAD src0_sel:WORD_1 src1_sel:DWORD
	v_and_b32_sdwa v5, v0, v231 dst_sel:DWORD dst_unused:UNUSED_PAD src0_sel:WORD_1 src1_sel:DWORD
	v_add3_u32 v0, v0, v5, s25
	v_add3_u32 v1, v1, v4, s25
	v_and_b32_sdwa v4, v3, v231 dst_sel:DWORD dst_unused:UNUSED_PAD src0_sel:WORD_1 src1_sel:DWORD
	v_and_b32_sdwa v5, v2, v231 dst_sel:DWORD dst_unused:UNUSED_PAD src0_sel:WORD_1 src1_sel:DWORD
	v_add3_u32 v3, v3, v4, s25
	v_add3_u32 v2, v2, v5, s25
	v_and_b32_e32 v3, 0xffff0000, v3
	v_and_b32_e32 v2, 0xffff0000, v2
	v_or_b32_sdwa v1, v3, v1 dst_sel:DWORD dst_unused:UNUSED_PAD src0_sel:DWORD src1_sel:WORD_1
	v_or_b32_sdwa v0, v2, v0 dst_sel:DWORD dst_unused:UNUSED_PAD src0_sel:DWORD src1_sel:WORD_1
	global_store_dwordx2 v[64:65], v[0:1], off offset:224
	v_mov_b32_e32 v0, v12
	v_mov_b32_e32 v1, v14
	v_pk_mul_f32 v[0:1], v[0:1], v[66:67] op_sel_hi:[1,0]
	v_mov_b32_e32 v14, v13
	v_pk_mul_f32 v[2:3], v[14:15], v[66:67] op_sel_hi:[1,0]
	v_and_b32_sdwa v4, v1, v231 dst_sel:DWORD dst_unused:UNUSED_PAD src0_sel:WORD_1 src1_sel:DWORD
	v_and_b32_sdwa v5, v0, v231 dst_sel:DWORD dst_unused:UNUSED_PAD src0_sel:WORD_1 src1_sel:DWORD
	v_add3_u32 v0, v0, v5, s25
	v_add3_u32 v1, v1, v4, s25
	v_and_b32_sdwa v4, v3, v231 dst_sel:DWORD dst_unused:UNUSED_PAD src0_sel:WORD_1 src1_sel:DWORD
	v_and_b32_sdwa v5, v2, v231 dst_sel:DWORD dst_unused:UNUSED_PAD src0_sel:WORD_1 src1_sel:DWORD
	v_add3_u32 v3, v3, v4, s25
	v_add3_u32 v2, v2, v5, s25
	v_and_b32_e32 v3, 0xffff0000, v3
	v_and_b32_e32 v2, 0xffff0000, v2
	v_or_b32_sdwa v1, v3, v1 dst_sel:DWORD dst_unused:UNUSED_PAD src0_sel:DWORD src1_sel:WORD_1
	v_or_b32_sdwa v0, v2, v0 dst_sel:DWORD dst_unused:UNUSED_PAD src0_sel:DWORD src1_sel:WORD_1
	global_store_dwordx2 v[64:65], v[0:1], off offset:240
	s_cbranch_scc0 .LBB0_1292
